# speedup vs baseline: 1.0159x; 1.0089x over previous
_ZN12_GLOBAL__N_112oproj_kernelEPKDF16_S1_PKfPf:
	s_load_dwordx8 s[4:11], s[0:1], 0x0
	s_lshl_b32 s1, s2, 4
	s_and_b32 s3, s1, 0x180
	s_lshr_b32 s1, s2, 2
	s_and_b32 s0, s2, 7
	s_and_b32 s1, s1, 0x1fffff8
	s_or_b32 s0, s1, s0
	s_lshl_b32 s0, s0, 7
	s_mov_b32 s1, 0
	s_lshl_b64 s[12:13], s[0:1], 10
	v_lshrrev_b32_e32 v36, 3, v0
	s_waitcnt lgkmcnt(0)
	v_and_b32_e32 v250, 0x5f, v0
	v_or_b32_e32 v250, s3, v250
	v_lshlrev_b32_e32 v250, 2, v250
	global_load_dword v251, v250, s[8:9]
	global_load_dword v252, v250, s[8:9] offset:128
	s_add_u32 s4, s4, s12
	s_addc_u32 s5, s5, s13
	v_lshlrev_b32_e32 v238, 10, v36
	v_mov_b32_e32 v239, 0
	v_lshlrev_b32_e32 v37, 4, v0
	v_lshl_add_u64 v[2:3], s[4:5], 0, v[238:239]
	v_and_b32_e32 v238, 0x70, v37
	v_lshl_add_u64 v[66:67], v[2:3], 0, v[238:239]
	s_mov_b32 s1, 0x8000
	v_add_co_u32_e32 v68, vcc, s1, v66
	s_mov_b32 s2, 0x10000
	s_nop 0
	v_addc_co_u32_e32 v69, vcc, 0, v67, vcc
	v_add_co_u32_e32 v70, vcc, s2, v66
	v_or_b32_e32 v1, s3, v36
	s_nop 0
	v_addc_co_u32_e32 v71, vcc, 0, v67, vcc
	s_mov_b32 s4, 0x18000
	v_add_co_u32_e32 v72, vcc, s4, v66
	v_lshl_add_u64 v[18:19], s[6:7], 0, v[238:239]
	v_lshlrev_b32_e32 v34, 10, v1
	v_mov_b32_e32 v35, v239
	v_addc_co_u32_e32 v73, vcc, 0, v67, vcc
	v_lshl_add_u64 v[74:75], v[18:19], 0, v[34:35]
	v_add_co_u32_e32 v76, vcc, s1, v74
	global_load_dwordx4 v[2:5], v[66:67], off
	global_load_dwordx4 v[6:9], v[68:69], off
	v_addc_co_u32_e32 v77, vcc, 0, v75, vcc
	v_add_co_u32_e32 v78, vcc, s2, v74
	global_load_dwordx4 v[10:13], v[70:71], off
	global_load_dwordx4 v[14:17], v[72:73], off
	v_addc_co_u32_e32 v79, vcc, 0, v75, vcc
	v_add_co_u32_e32 v80, vcc, s4, v74
	global_load_dwordx4 v[18:21], v[74:75], off
	global_load_dwordx4 v[22:25], v[76:77], off
	v_addc_co_u32_e32 v81, vcc, 0, v75, vcc
	global_load_dwordx4 v[26:29], v[78:79], off
	global_load_dwordx4 v[30:33], v[80:81], off
	v_lshl_add_u64 v[34:35], s[6:7], 0, v[34:35]
	s_movk_i32 s5, 0x70
	v_xor_b32_e32 v37, v37, v0
	v_lshlrev_b32_e32 v36, 7, v36
	v_lshl_add_u64 v[34:35], v[34:35], 0, v[238:239]
	v_and_or_b32 v82, v37, s5, v36
	v_add_co_u32_e32 v36, vcc, s1, v34
	global_load_dwordx4 v[100:103], v[66:67], off offset:128
	global_load_dwordx4 v[104:107], v[68:69], off offset:128
	global_load_dwordx4 v[112:115], v[70:71], off offset:128
	global_load_dwordx4 v[116:119], v[72:73], off offset:128
	v_addc_co_u32_e32 v37, vcc, 0, v35, vcc
	global_load_dwordx4 v[120:123], v[34:35], off offset:128
	global_load_dwordx4 v[124:127], v[36:37], off offset:128
	v_add_co_u32_e32 v36, vcc, s2, v34
	v_lshrrev_b32_e32 v1, 1, v0
	s_nop 0
	v_addc_co_u32_e32 v37, vcc, 0, v35, vcc
	v_add_co_u32_e32 v34, vcc, s4, v34
	v_lshrrev_b32_e32 v38, 5, v0
	s_nop 0
	v_addc_co_u32_e32 v35, vcc, 0, v35, vcc
	global_load_dwordx4 v[128:131], v[36:37], off offset:128
	global_load_dwordx4 v[132:135], v[34:35], off offset:128
	v_and_b32_e32 v1, 64, v1
	v_bfe_u32 v144, v0, 1, 3
	v_and_or_b32 v39, v0, 31, v1
	v_lshlrev_b32_e32 v87, 7, v39
	v_bfe_u32 v240, v0, 5, 1
	v_bitop3_b32 v85, v240, v144, 2 bitop3:0x36
	v_lshlrev_b32_e32 v86, 4, v85
	v_or_b32_e32 v85, v87, v86
	v_mov_b32_e32 v241, v239
	s_waitcnt vmcnt(15)
	ds_write_b128 v82, v[2:5]
	s_waitcnt vmcnt(14)
	ds_write_b128 v82, v[6:9] offset:4096
	s_waitcnt vmcnt(13)
	ds_write_b128 v82, v[10:13] offset:8192
	s_waitcnt vmcnt(12)
	ds_write_b128 v82, v[14:17] offset:12288
	s_waitcnt vmcnt(11)
	ds_write_b128 v82, v[18:21] offset:16384
	s_waitcnt vmcnt(10)
	ds_write_b128 v82, v[22:25] offset:20480
	s_waitcnt vmcnt(9)
	ds_write_b128 v82, v[26:29] offset:24576
	s_waitcnt vmcnt(8)
	ds_write_b128 v82, v[30:33] offset:28672
	v_bitop3_b32 v2, v38, v144, 1 bitop3:0x6c
	v_lshlrev_b32_e32 v6, 4, v2
	v_or_b32_e32 v83, v87, v6
	s_waitcnt lgkmcnt(0)
	s_barrier
	ds_read_b128 v[2:5], v83
	v_lshlrev_b32_e32 v7, 7, v0
	v_and_b32_e32 v145, 0x2f80, v7
	v_or_b32_e32 v84, v145, v6
	ds_read_b128 v[6:9], v84 offset:16384
	ds_read_b128 v[10:13], v83 offset:4096
	ds_read_b128 v[14:17], v84 offset:20480
	ds_read_b128 v[88:91], v85
	s_waitcnt lgkmcnt(3)
	v_mfma_f32_32x32x16_f16 v[50:65], v[2:5], v[6:9], 0
	v_or_b32_e32 v86, v145, v86
	ds_read_b128 v[92:95], v86 offset:16384
	ds_read_b128 v[96:99], v85 offset:4096
	ds_read_b128 v[108:111], v86 offset:20480
	v_and_b32_e32 v0, 0x5f, v0
	v_or_b32_e32 v0, s3, v0
	v_lshlrev_b32_e32 v238, 2, v0
	v_lshlrev_b32_e32 v0, 2, v240
	s_waitcnt lgkmcnt(4)
	v_mfma_f32_32x32x16_f16 v[18:33], v[2:5], v[14:17], 0
	v_mfma_f32_32x32x16_f16 v[34:49], v[10:13], v[6:9], 0
	v_mfma_f32_32x32x16_f16 v[2:17], v[10:13], v[14:17], 0
	s_waitcnt lgkmcnt(2)
	v_mfma_f32_32x32x16_f16 v[50:65], v[88:91], v[92:95], v[50:65]
	s_waitcnt lgkmcnt(0)
	v_mfma_f32_32x32x16_f16 v[18:33], v[88:91], v[108:111], v[18:33]
	v_bitop3_b32 v88, v240, v144, 4 bitop3:0x36
	v_lshlrev_b32_e32 v88, 4, v88
	v_or_b32_e32 v90, v87, v88
	v_mfma_f32_32x32x16_f16 v[34:49], v[96:99], v[92:95], v[34:49]
	v_or_b32_e32 v94, v145, v88
	v_bitop3_b32 v88, v240, v144, 6 bitop3:0x36
	v_lshlrev_b32_e32 v88, 4, v88
	v_or3_b32 v240, s0, v1, v0
	v_lshl_add_u64 v[0:1], s[10:11], 0, v[238:239]
	v_mfma_f32_32x32x16_f16 v[2:17], v[96:99], v[108:111], v[2:17]
	ds_read_b128 v[96:99], v90
	ds_read_b128 v[108:111], v94 offset:16384
	ds_read_b128 v[136:139], v90 offset:4096
	ds_read_b128 v[140:143], v94 offset:20480
	s_waitcnt lgkmcnt(2)
	v_mfma_f32_32x32x16_f16 v[50:65], v[96:99], v[108:111], v[50:65]
	s_waitcnt lgkmcnt(0)
	v_mfma_f32_32x32x16_f16 v[18:33], v[96:99], v[140:143], v[18:33]
	v_or_b32_e32 v98, v87, v88
	v_mfma_f32_32x32x16_f16 v[34:49], v[136:139], v[108:111], v[34:49]
	v_or_b32_e32 v110, v145, v88
	v_mfma_f32_32x32x16_f16 v[2:17], v[136:139], v[140:143], v[2:17]
	ds_read_b128 v[136:139], v98
	ds_read_b128 v[140:143], v110 offset:16384
	ds_read_b128 v[144:147], v98 offset:4096
	ds_read_b128 v[148:151], v110 offset:20480
	s_waitcnt lgkmcnt(2)
	v_mfma_f32_32x32x16_f16 v[50:65], v[136:139], v[140:143], v[50:65]
	s_waitcnt lgkmcnt(0)
	v_mfma_f32_32x32x16_f16 v[18:33], v[136:139], v[148:151], v[18:33]
	v_mfma_f32_32x32x16_f16 v[34:49], v[144:147], v[140:143], v[34:49]
	global_load_dwordx4 v[136:139], v[66:67], off offset:256
	global_load_dwordx4 v[140:143], v[68:69], off offset:256
	global_load_dwordx4 v[152:155], v[70:71], off offset:256
	global_load_dwordx4 v[156:159], v[72:73], off offset:256
	global_load_dwordx4 v[160:163], v[74:75], off offset:256
	global_load_dwordx4 v[164:167], v[76:77], off offset:256
	global_load_dwordx4 v[168:171], v[78:79], off offset:256
	global_load_dwordx4 v[172:175], v[80:81], off offset:256
	s_waitcnt vmcnt(15)
	ds_write_b128 v82, v[100:103] offset:32768
	s_waitcnt vmcnt(14)
	ds_write_b128 v82, v[104:107] offset:36864
	s_waitcnt vmcnt(13)
	ds_write_b128 v82, v[112:115] offset:40960
	s_waitcnt vmcnt(12)
	ds_write_b128 v82, v[116:119] offset:45056
	s_waitcnt vmcnt(11)
	ds_write_b128 v82, v[120:123] offset:49152
	s_waitcnt vmcnt(10)
	ds_write_b128 v82, v[124:127] offset:53248
	s_waitcnt vmcnt(9)
	ds_write_b128 v82, v[128:131] offset:57344
	s_waitcnt vmcnt(8)
	ds_write_b128 v82, v[132:135] offset:61440
	s_waitcnt lgkmcnt(0)
	s_barrier
	ds_read_b128 v[100:103], v83 offset:32768
	ds_read_b128 v[104:107], v84 offset:49152
	ds_read_b128 v[112:115], v83 offset:36864
	ds_read_b128 v[116:119], v84 offset:53248
	v_mfma_f32_32x32x16_f16 v[2:17], v[144:147], v[148:151], v[2:17]
	s_waitcnt lgkmcnt(2)
	v_mfma_f32_32x32x16_f16 v[50:65], v[100:103], v[104:107], v[50:65]
	s_waitcnt lgkmcnt(0)
	v_mfma_f32_32x32x16_f16 v[18:33], v[100:103], v[116:119], v[18:33]
	v_mfma_f32_32x32x16_f16 v[34:49], v[112:115], v[104:107], v[34:49]
	v_mfma_f32_32x32x16_f16 v[2:17], v[112:115], v[116:119], v[2:17]
	ds_read_b128 v[100:103], v85 offset:32768
	ds_read_b128 v[104:107], v86 offset:49152
	ds_read_b128 v[112:115], v85 offset:36864
	ds_read_b128 v[116:119], v86 offset:53248
	s_waitcnt lgkmcnt(2)
	v_mfma_f32_32x32x16_f16 v[50:65], v[100:103], v[104:107], v[50:65]
	s_waitcnt lgkmcnt(0)
	v_mfma_f32_32x32x16_f16 v[18:33], v[100:103], v[116:119], v[18:33]
	v_mfma_f32_32x32x16_f16 v[34:49], v[112:115], v[104:107], v[34:49]
	v_mfma_f32_32x32x16_f16 v[2:17], v[112:115], v[116:119], v[2:17]
	ds_read_b128 v[100:103], v90 offset:32768
	ds_read_b128 v[104:107], v94 offset:49152
	ds_read_b128 v[112:115], v90 offset:36864
	ds_read_b128 v[116:119], v94 offset:53248
	s_waitcnt lgkmcnt(2)
	v_mfma_f32_32x32x16_f16 v[50:65], v[100:103], v[104:107], v[50:65]
	s_waitcnt lgkmcnt(0)
	v_mfma_f32_32x32x16_f16 v[18:33], v[100:103], v[116:119], v[18:33]
	v_mfma_f32_32x32x16_f16 v[34:49], v[112:115], v[104:107], v[34:49]
	v_mfma_f32_32x32x16_f16 v[2:17], v[112:115], v[116:119], v[2:17]
	ds_read_b128 v[100:103], v98 offset:32768
	ds_read_b128 v[104:107], v110 offset:49152
	ds_read_b128 v[112:115], v98 offset:36864
	ds_read_b128 v[116:119], v110 offset:53248
	s_waitcnt lgkmcnt(2)
	v_mfma_f32_32x32x16_f16 v[50:65], v[100:103], v[104:107], v[50:65]
	s_waitcnt lgkmcnt(0)
	v_mfma_f32_32x32x16_f16 v[18:33], v[100:103], v[116:119], v[18:33]
	v_mfma_f32_32x32x16_f16 v[34:49], v[112:115], v[104:107], v[34:49]
	global_load_dwordx4 v[100:103], v[66:67], off offset:384
	global_load_dwordx4 v[104:107], v[68:69], off offset:384
	global_load_dwordx4 v[120:123], v[70:71], off offset:384
	global_load_dwordx4 v[124:127], v[72:73], off offset:384
	global_load_dwordx4 v[128:131], v[74:75], off offset:384
	global_load_dwordx4 v[132:135], v[76:77], off offset:384
	global_load_dwordx4 v[144:147], v[78:79], off offset:384
	global_load_dwordx4 v[148:151], v[80:81], off offset:384
	s_waitcnt vmcnt(15)
	ds_write_b128 v82, v[136:139]
	s_waitcnt vmcnt(14)
	ds_write_b128 v82, v[140:143] offset:4096
	s_waitcnt vmcnt(13)
	ds_write_b128 v82, v[152:155] offset:8192
	s_waitcnt vmcnt(12)
	ds_write_b128 v82, v[156:159] offset:12288
	s_waitcnt vmcnt(11)
	ds_write_b128 v82, v[160:163] offset:16384
	s_waitcnt vmcnt(10)
	ds_write_b128 v82, v[164:167] offset:20480
	s_waitcnt vmcnt(9)
	ds_write_b128 v82, v[168:171] offset:24576
	s_waitcnt vmcnt(8)
	ds_write_b128 v82, v[172:175] offset:28672
	s_waitcnt lgkmcnt(0)
	s_barrier
	v_mfma_f32_32x32x16_f16 v[2:17], v[112:115], v[116:119], v[2:17]
	ds_read_b128 v[112:115], v83
	ds_read_b128 v[116:119], v84 offset:16384
	ds_read_b128 v[136:139], v83 offset:4096
	ds_read_b128 v[140:143], v84 offset:20480
	s_waitcnt lgkmcnt(2)
	v_mfma_f32_32x32x16_f16 v[50:65], v[112:115], v[116:119], v[50:65]
	s_waitcnt lgkmcnt(0)
	v_mfma_f32_32x32x16_f16 v[18:33], v[112:115], v[140:143], v[18:33]
	v_mfma_f32_32x32x16_f16 v[34:49], v[136:139], v[116:119], v[34:49]
	v_mfma_f32_32x32x16_f16 v[2:17], v[136:139], v[140:143], v[2:17]
	ds_read_b128 v[112:115], v85
	ds_read_b128 v[116:119], v86 offset:16384
	ds_read_b128 v[136:139], v85 offset:4096
	ds_read_b128 v[140:143], v86 offset:20480
	s_waitcnt lgkmcnt(2)
	v_mfma_f32_32x32x16_f16 v[50:65], v[112:115], v[116:119], v[50:65]
	s_waitcnt lgkmcnt(0)
	v_mfma_f32_32x32x16_f16 v[18:33], v[112:115], v[140:143], v[18:33]
	v_mfma_f32_32x32x16_f16 v[34:49], v[136:139], v[116:119], v[34:49]
	v_mfma_f32_32x32x16_f16 v[2:17], v[136:139], v[140:143], v[2:17]
	ds_read_b128 v[112:115], v90
	ds_read_b128 v[116:119], v94 offset:16384
	ds_read_b128 v[136:139], v90 offset:4096
	ds_read_b128 v[140:143], v94 offset:20480
	s_waitcnt lgkmcnt(2)
	v_mfma_f32_32x32x16_f16 v[50:65], v[112:115], v[116:119], v[50:65]
	s_waitcnt lgkmcnt(0)
	v_mfma_f32_32x32x16_f16 v[18:33], v[112:115], v[140:143], v[18:33]
	v_mfma_f32_32x32x16_f16 v[34:49], v[136:139], v[116:119], v[34:49]
	v_mfma_f32_32x32x16_f16 v[2:17], v[136:139], v[140:143], v[2:17]
	ds_read_b128 v[112:115], v98
	ds_read_b128 v[116:119], v110 offset:16384
	ds_read_b128 v[136:139], v98 offset:4096
	ds_read_b128 v[140:143], v110 offset:20480
	s_waitcnt lgkmcnt(2)
	v_mfma_f32_32x32x16_f16 v[50:65], v[112:115], v[116:119], v[50:65]
	s_waitcnt lgkmcnt(0)
	v_mfma_f32_32x32x16_f16 v[18:33], v[112:115], v[140:143], v[18:33]
	v_mfma_f32_32x32x16_f16 v[34:49], v[136:139], v[116:119], v[34:49]
	global_load_dwordx4 v[112:115], v[66:67], off offset:512
	global_load_dwordx4 v[116:119], v[68:69], off offset:512
	global_load_dwordx4 v[152:155], v[70:71], off offset:512
	global_load_dwordx4 v[156:159], v[72:73], off offset:512
	global_load_dwordx4 v[160:163], v[74:75], off offset:512
	global_load_dwordx4 v[164:167], v[76:77], off offset:512
	global_load_dwordx4 v[168:171], v[78:79], off offset:512
	global_load_dwordx4 v[172:175], v[80:81], off offset:512
	s_waitcnt vmcnt(15)
	ds_write_b128 v82, v[100:103] offset:32768
	s_waitcnt vmcnt(14)
	ds_write_b128 v82, v[104:107] offset:36864
	s_waitcnt vmcnt(13)
	ds_write_b128 v82, v[120:123] offset:40960
	s_waitcnt vmcnt(12)
	ds_write_b128 v82, v[124:127] offset:45056
	s_waitcnt vmcnt(11)
	ds_write_b128 v82, v[128:131] offset:49152
	s_waitcnt vmcnt(10)
	ds_write_b128 v82, v[132:135] offset:53248
	s_waitcnt vmcnt(9)
	ds_write_b128 v82, v[144:147] offset:57344
	s_waitcnt vmcnt(8)
	ds_write_b128 v82, v[148:151] offset:61440
	s_waitcnt lgkmcnt(0)
	s_barrier
	ds_read_b128 v[100:103], v83 offset:32768
	ds_read_b128 v[104:107], v84 offset:49152
	ds_read_b128 v[120:123], v83 offset:36864
	ds_read_b128 v[124:127], v84 offset:53248
	v_mfma_f32_32x32x16_f16 v[2:17], v[136:139], v[140:143], v[2:17]
	s_waitcnt lgkmcnt(2)
	v_mfma_f32_32x32x16_f16 v[50:65], v[100:103], v[104:107], v[50:65]
	s_waitcnt lgkmcnt(0)
	v_mfma_f32_32x32x16_f16 v[18:33], v[100:103], v[124:127], v[18:33]
	v_mfma_f32_32x32x16_f16 v[34:49], v[120:123], v[104:107], v[34:49]
	v_mfma_f32_32x32x16_f16 v[2:17], v[120:123], v[124:127], v[2:17]
	ds_read_b128 v[100:103], v85 offset:32768
	ds_read_b128 v[104:107], v86 offset:49152
	ds_read_b128 v[120:123], v85 offset:36864
	ds_read_b128 v[124:127], v86 offset:53248
	s_waitcnt lgkmcnt(2)
	v_mfma_f32_32x32x16_f16 v[50:65], v[100:103], v[104:107], v[50:65]
	s_waitcnt lgkmcnt(0)
	v_mfma_f32_32x32x16_f16 v[18:33], v[100:103], v[124:127], v[18:33]
	v_mfma_f32_32x32x16_f16 v[34:49], v[120:123], v[104:107], v[34:49]
	v_mfma_f32_32x32x16_f16 v[2:17], v[120:123], v[124:127], v[2:17]
	ds_read_b128 v[100:103], v90 offset:32768
	ds_read_b128 v[104:107], v94 offset:49152
	ds_read_b128 v[120:123], v90 offset:36864
	ds_read_b128 v[124:127], v94 offset:53248
	s_waitcnt lgkmcnt(2)
	v_mfma_f32_32x32x16_f16 v[50:65], v[100:103], v[104:107], v[50:65]
	s_waitcnt lgkmcnt(0)
	v_mfma_f32_32x32x16_f16 v[18:33], v[100:103], v[124:127], v[18:33]
	v_mfma_f32_32x32x16_f16 v[34:49], v[120:123], v[104:107], v[34:49]
	v_mfma_f32_32x32x16_f16 v[2:17], v[120:123], v[124:127], v[2:17]
	ds_read_b128 v[100:103], v98 offset:32768
	ds_read_b128 v[104:107], v110 offset:49152
	ds_read_b128 v[120:123], v98 offset:36864
	ds_read_b128 v[124:127], v110 offset:53248
	s_waitcnt lgkmcnt(2)
	v_mfma_f32_32x32x16_f16 v[50:65], v[100:103], v[104:107], v[50:65]
	s_waitcnt lgkmcnt(0)
	v_mfma_f32_32x32x16_f16 v[18:33], v[100:103], v[124:127], v[18:33]
	v_mfma_f32_32x32x16_f16 v[34:49], v[120:123], v[104:107], v[34:49]
	global_load_dwordx4 v[100:103], v[66:67], off offset:640
	global_load_dwordx4 v[104:107], v[68:69], off offset:640
	global_load_dwordx4 v[128:131], v[70:71], off offset:640
	global_load_dwordx4 v[132:135], v[72:73], off offset:640
	global_load_dwordx4 v[136:139], v[74:75], off offset:640
	global_load_dwordx4 v[140:143], v[76:77], off offset:640
	global_load_dwordx4 v[144:147], v[78:79], off offset:640
	global_load_dwordx4 v[148:151], v[80:81], off offset:640
	s_waitcnt vmcnt(15)
	ds_write_b128 v82, v[112:115]
	s_waitcnt vmcnt(14)
	ds_write_b128 v82, v[116:119] offset:4096
	s_waitcnt vmcnt(13)
	ds_write_b128 v82, v[152:155] offset:8192
	s_waitcnt vmcnt(12)
	ds_write_b128 v82, v[156:159] offset:12288
	s_waitcnt vmcnt(11)
	ds_write_b128 v82, v[160:163] offset:16384
	s_waitcnt vmcnt(10)
	ds_write_b128 v82, v[164:167] offset:20480
	s_waitcnt vmcnt(9)
	ds_write_b128 v82, v[168:171] offset:24576
	s_waitcnt vmcnt(8)
	ds_write_b128 v82, v[172:175] offset:28672
	s_waitcnt lgkmcnt(0)
	s_barrier
	v_mfma_f32_32x32x16_f16 v[2:17], v[120:123], v[124:127], v[2:17]
	ds_read_b128 v[112:115], v83
	ds_read_b128 v[116:119], v84 offset:16384
	ds_read_b128 v[120:123], v83 offset:4096
	ds_read_b128 v[124:127], v84 offset:20480
	s_waitcnt lgkmcnt(2)
	v_mfma_f32_32x32x16_f16 v[50:65], v[112:115], v[116:119], v[50:65]
	s_waitcnt lgkmcnt(0)
	v_mfma_f32_32x32x16_f16 v[18:33], v[112:115], v[124:127], v[18:33]
	v_mfma_f32_32x32x16_f16 v[34:49], v[120:123], v[116:119], v[34:49]
	v_mfma_f32_32x32x16_f16 v[2:17], v[120:123], v[124:127], v[2:17]
	ds_read_b128 v[112:115], v85
	ds_read_b128 v[116:119], v86 offset:16384
	ds_read_b128 v[120:123], v85 offset:4096
	ds_read_b128 v[124:127], v86 offset:20480
	s_waitcnt lgkmcnt(2)
	v_mfma_f32_32x32x16_f16 v[50:65], v[112:115], v[116:119], v[50:65]
	s_waitcnt lgkmcnt(0)
	v_mfma_f32_32x32x16_f16 v[18:33], v[112:115], v[124:127], v[18:33]
	v_mfma_f32_32x32x16_f16 v[34:49], v[120:123], v[116:119], v[34:49]
	v_mfma_f32_32x32x16_f16 v[2:17], v[120:123], v[124:127], v[2:17]
	ds_read_b128 v[112:115], v90
	ds_read_b128 v[116:119], v94 offset:16384
	ds_read_b128 v[120:123], v90 offset:4096
	ds_read_b128 v[124:127], v94 offset:20480
	s_waitcnt lgkmcnt(2)
	v_mfma_f32_32x32x16_f16 v[50:65], v[112:115], v[116:119], v[50:65]
	s_waitcnt lgkmcnt(0)
	v_mfma_f32_32x32x16_f16 v[18:33], v[112:115], v[124:127], v[18:33]
	v_mfma_f32_32x32x16_f16 v[34:49], v[120:123], v[116:119], v[34:49]
	v_mfma_f32_32x32x16_f16 v[2:17], v[120:123], v[124:127], v[2:17]
	ds_read_b128 v[112:115], v98
	ds_read_b128 v[116:119], v110 offset:16384
	ds_read_b128 v[120:123], v98 offset:4096
	ds_read_b128 v[124:127], v110 offset:20480
	global_load_dwordx4 v[152:155], v[66:67], off offset:768
	global_load_dwordx4 v[156:159], v[68:69], off offset:768
	global_load_dwordx4 v[160:163], v[70:71], off offset:768
	global_load_dwordx4 v[164:167], v[72:73], off offset:768
	global_load_dwordx4 v[168:171], v[74:75], off offset:768
	global_load_dwordx4 v[172:175], v[76:77], off offset:768
	global_load_dwordx4 v[176:179], v[78:79], off offset:768
	global_load_dwordx4 v[206:209], v[80:81], off offset:768
	s_waitcnt vmcnt(15)
	ds_write_b128 v82, v[100:103] offset:32768
	s_waitcnt vmcnt(14)
	ds_write_b128 v82, v[104:107] offset:36864
	s_waitcnt vmcnt(13)
	ds_write_b128 v82, v[128:131] offset:40960
	s_waitcnt vmcnt(12)
	ds_write_b128 v82, v[132:135] offset:45056
	s_waitcnt vmcnt(11)
	ds_write_b128 v82, v[136:139] offset:49152
	s_waitcnt vmcnt(10)
	ds_write_b128 v82, v[140:143] offset:53248
	s_waitcnt vmcnt(9)
	ds_write_b128 v82, v[144:147] offset:57344
	s_waitcnt vmcnt(8)
	ds_write_b128 v82, v[148:151] offset:61440
	s_waitcnt lgkmcnt(0)
	s_barrier
	v_mfma_f32_32x32x16_f16 v[50:65], v[112:115], v[116:119], v[50:65]
	v_mfma_f32_32x32x16_f16 v[18:33], v[112:115], v[124:127], v[18:33]
	v_mfma_f32_32x32x16_f16 v[34:49], v[120:123], v[116:119], v[34:49]
	ds_read_b128 v[100:103], v83 offset:32768
	ds_read_b128 v[104:107], v84 offset:49152
	ds_read_b128 v[112:115], v83 offset:36864
	ds_read_b128 v[116:119], v84 offset:53248
	global_load_dwordx4 v[222:225], v[66:67], off offset:896
	global_load_dwordx4 v[226:229], v[68:69], off offset:896
	ds_read_b128 v[66:69], v85 offset:32768
	global_load_dwordx4 v[230:233], v[70:71], off offset:896
	global_load_dwordx4 v[234:237], v[72:73], off offset:896
	ds_read_b128 v[202:205], v86 offset:49152
	global_load_dwordx4 v[242:245], v[74:75], off offset:896
	s_nop 0
	global_load_dwordx4 v[74:77], v[76:77], off offset:896
	ds_read_b128 v[186:189], v85 offset:36864
	ds_read_b128 v[190:193], v86 offset:53248
	global_load_dwordx4 v[246:249], v[78:79], off offset:896
	s_nop 0
	global_load_dwordx4 v[78:81], v[80:81], off offset:896
	s_waitcnt lgkmcnt(6)
	v_mfma_f32_32x32x16_f16 v[50:65], v[100:103], v[104:107], v[50:65]
	v_mfma_f32_32x32x16_f16 v[2:17], v[120:123], v[124:127], v[2:17]
	s_waitcnt lgkmcnt(4)
	v_mfma_f32_32x32x16_f16 v[18:33], v[100:103], v[116:119], v[18:33]
	s_waitcnt lgkmcnt(2)
	v_mfma_f32_32x32x16_f16 v[50:65], v[66:69], v[202:205], v[50:65]
	v_mfma_f32_32x32x16_f16 v[34:49], v[112:115], v[104:107], v[34:49]
	v_mfma_f32_32x32x16_f16 v[2:17], v[112:115], v[116:119], v[2:17]
	ds_read_b128 v[198:201], v90 offset:32768
	ds_read_b128 v[114:117], v90 offset:36864
	ds_read_b128 v[182:185], v94 offset:49152
	ds_read_b128 v[122:125], v94 offset:53248
	ds_read_b128 v[130:133], v98 offset:32768
	ds_read_b128 v[102:105], v98 offset:36864
	ds_read_b128 v[194:197], v110 offset:49152
	ds_read_b128 v[106:109], v110 offset:53248
	s_waitcnt vmcnt(15)
	ds_write_b128 v82, v[152:155]
	s_waitcnt vmcnt(14)
	ds_write_b128 v82, v[156:159] offset:4096
	s_waitcnt vmcnt(13)
	ds_write_b128 v82, v[160:163] offset:8192
	s_waitcnt vmcnt(12)
	ds_write_b128 v82, v[164:167] offset:12288
	s_waitcnt lgkmcnt(12)
	v_mfma_f32_32x32x16_f16 v[18:33], v[66:69], v[190:193], v[18:33]
	s_waitcnt vmcnt(11)
	ds_write_b128 v82, v[168:171] offset:16384
	s_waitcnt vmcnt(10)
	ds_write_b128 v82, v[172:175] offset:20480
	s_waitcnt vmcnt(9)
	ds_write_b128 v82, v[176:179] offset:24576
	s_waitcnt vmcnt(8)
	ds_write_b128 v82, v[206:209] offset:28672
	s_waitcnt lgkmcnt(0)
	s_barrier
	ds_read_b128 v[162:165], v83
	ds_read_b128 v[206:209], v84 offset:16384
	ds_read_b128 v[150:153], v83 offset:4096
	ds_read_b128 v[154:157], v84 offset:20480
	ds_read_b128 v[158:161], v85
	ds_read_b128 v[134:137], v85 offset:4096
	ds_read_b128 v[210:213], v86 offset:16384
	ds_read_b128 v[142:145], v86 offset:20480
	ds_read_b128 v[146:149], v90
	ds_read_b128 v[118:121], v90 offset:4096
	ds_read_b128 v[214:217], v94 offset:16384
	ds_read_b128 v[126:129], v94 offset:20480
	ds_read_b128 v[138:141], v98
	ds_read_b128 v[66:69], v98 offset:4096
	ds_read_b128 v[218:221], v110 offset:16384
	ds_read_b128 v[70:73], v110 offset:20480
	v_mfma_f32_32x32x16_f16 v[50:65], v[198:201], v[182:185], v[50:65]
	s_waitcnt vmcnt(7)
	ds_write_b128 v82, v[222:225] offset:32768
	s_waitcnt vmcnt(6)
	ds_write_b128 v82, v[226:229] offset:36864
	s_waitcnt vmcnt(5)
	ds_write_b128 v82, v[230:233] offset:40960
	s_waitcnt vmcnt(4)
	ds_write_b128 v82, v[234:237] offset:45056
	s_waitcnt vmcnt(3)
	ds_write_b128 v82, v[242:245] offset:49152
	s_waitcnt vmcnt(2)
	ds_write_b128 v82, v[74:77] offset:53248
	s_waitcnt vmcnt(1)
	ds_write_b128 v82, v[246:249] offset:57344
	s_waitcnt vmcnt(0)
	ds_write_b128 v82, v[78:81] offset:61440
	s_waitcnt lgkmcnt(0)
	s_barrier
	ds_read_b128 v[166:169], v83 offset:32768
	ds_read_b128 v[222:225], v84 offset:49152
	ds_read_b128 v[74:77], v83 offset:36864
	ds_read_b128 v[78:81], v84 offset:53248
	ds_read_b128 v[170:173], v85 offset:32768
	ds_read_b128 v[82:85], v85 offset:36864
	ds_read_b128 v[226:229], v86 offset:49152
	ds_read_b128 v[86:89], v86 offset:53248
	ds_read_b128 v[174:177], v90 offset:32768
	ds_read_b128 v[90:93], v90 offset:36864
	ds_read_b128 v[230:233], v94 offset:49152
	ds_read_b128 v[94:97], v94 offset:53248
	ds_read_b128 v[178:181], v98 offset:32768
	ds_read_b128 v[98:101], v98 offset:36864
	ds_read_b128 v[234:237], v110 offset:49152
	ds_read_b128 v[110:113], v110 offset:53248
	s_waitcnt lgkmcnt(0)
	s_barrier
	v_mfma_f32_32x32x16_f16 v[50:65], v[130:133], v[194:197], v[50:65]
	v_lshlrev_b64 v[242:243], 11, v[240:241]
	v_lshl_add_u64 v[242:243], v[0:1], 0, v[242:243]
	v_or_b32_e32 v238, 59, v240
	v_mfma_f32_32x32x16_f16 v[50:65], v[162:165], v[206:209], v[50:65]
	v_mfma_f32_32x32x16_f16 v[50:65], v[158:161], v[210:213], v[50:65]
	v_mfma_f32_32x32x16_f16 v[50:65], v[146:149], v[214:217], v[50:65]
	v_mfma_f32_32x32x16_f16 v[50:65], v[138:141], v[218:221], v[50:65]
	v_mfma_f32_32x32x16_f16 v[34:49], v[186:189], v[202:205], v[34:49]
	v_mov_b32_e32 v203, v239
	v_mfma_f32_32x32x16_f16 v[50:65], v[166:169], v[222:225], v[50:65]
	v_mfma_f32_32x32x16_f16 v[34:49], v[114:117], v[182:185], v[34:49]
	v_mov_b32_e32 v185, v239
	v_mfma_f32_32x32x16_f16 v[50:65], v[170:173], v[226:229], v[50:65]
	v_mfma_f32_32x32x16_f16 v[34:49], v[102:105], v[194:197], v[34:49]
	v_mov_b32_e32 v195, v239
	v_mov_b32_e32 v197, v239
	v_mfma_f32_32x32x16_f16 v[50:65], v[174:177], v[230:233], v[50:65]
	v_mfma_f32_32x32x16_f16 v[34:49], v[150:153], v[206:209], v[34:49]
	v_mfma_f32_32x32x16_f16 v[2:17], v[186:189], v[190:193], v[2:17]
	v_mov_b32_e32 v189, v239
	v_mov_b32_e32 v191, v239
	v_mov_b32_e32 v193, v239
	v_mfma_f32_32x32x16_f16 v[50:65], v[178:181], v[234:237], v[50:65]
	v_mfma_f32_32x32x16_f16 v[34:49], v[134:137], v[210:213], v[34:49]
	s_waitcnt vmcnt(1)
	s_nop 9
	v_add_f32_e32 v50, v251, v50
	global_store_dword v[242:243], v50, off sc1
	v_or_b32_e32 v50, 1, v240
	v_add_f32_e32 v202, v251, v51
	v_mov_b32_e32 v51, v239
	v_lshlrev_b64 v[50:51], 11, v[50:51]
	v_lshl_add_u64 v[50:51], v[0:1], 0, v[50:51]
	v_mfma_f32_32x32x16_f16 v[18:33], v[198:201], v[122:125], v[18:33]
	global_store_dword v[50:51], v202, off sc1
	v_or_b32_e32 v202, 2, v240
	v_lshlrev_b64 v[186:187], 11, v[202:203]
	v_add_f32_e32 v52, v251, v52
	v_lshl_add_u64 v[186:187], v[0:1], 0, v[186:187]
	global_store_dword v[186:187], v52, off sc1
	v_or_b32_e32 v52, 3, v240
	v_mfma_f32_32x32x16_f16 v[2:17], v[114:117], v[122:125], v[2:17]
	v_add_f32_e32 v188, v251, v53
	v_mov_b32_e32 v53, v239
	v_lshlrev_b64 v[52:53], 11, v[52:53]
	v_lshl_add_u64 v[52:53], v[0:1], 0, v[52:53]
	global_store_dword v[52:53], v188, off sc1
	v_or_b32_e32 v188, 8, v240
	v_lshlrev_b64 v[188:189], 11, v[188:189]
	v_mfma_f32_32x32x16_f16 v[34:49], v[118:121], v[214:217], v[34:49]
	v_add_f32_e32 v54, v251, v54
	v_lshl_add_u64 v[182:183], v[0:1], 0, v[188:189]
	global_store_dword v[182:183], v54, off sc1
	v_or_b32_e32 v54, 9, v240
	v_add_f32_e32 v184, v251, v55
	v_mov_b32_e32 v55, v239
	v_lshlrev_b64 v[54:55], 11, v[54:55]
	v_mfma_f32_32x32x16_f16 v[18:33], v[130:133], v[106:109], v[18:33]
	v_lshl_add_u64 v[54:55], v[0:1], 0, v[54:55]
	global_store_dword v[54:55], v184, off sc1
	v_or_b32_e32 v184, 10, v240
	v_lshlrev_b64 v[184:185], 11, v[184:185]
	v_add_f32_e32 v56, v251, v56
	v_lshl_add_u64 v[184:185], v[0:1], 0, v[184:185]
	global_store_dword v[184:185], v56, off sc1
	v_mfma_f32_32x32x16_f16 v[2:17], v[102:105], v[106:109], v[2:17]
	v_or_b32_e32 v56, 11, v240
	v_add_f32_e32 v188, v251, v57
	v_mov_b32_e32 v57, v239
	v_lshlrev_b64 v[56:57], 11, v[56:57]
	v_lshl_add_u64 v[56:57], v[0:1], 0, v[56:57]
	global_store_dword v[56:57], v188, off sc1
	v_or_b32_e32 v188, 16, v240
	v_mfma_f32_32x32x16_f16 v[34:49], v[66:69], v[218:221], v[34:49]
	v_mov_b32_e32 v189, v239
	v_lshlrev_b64 v[188:189], 11, v[188:189]
	v_add_f32_e32 v58, v251, v58
	v_lshl_add_u64 v[188:189], v[0:1], 0, v[188:189]
	global_store_dword v[188:189], v58, off sc1
	v_or_b32_e32 v58, 17, v240
	v_add_f32_e32 v190, v251, v59
	v_mfma_f32_32x32x16_f16 v[18:33], v[162:165], v[154:157], v[18:33]
	v_mov_b32_e32 v59, v239
	v_lshlrev_b64 v[58:59], 11, v[58:59]
	v_lshl_add_u64 v[58:59], v[0:1], 0, v[58:59]
	global_store_dword v[58:59], v190, off sc1
	v_or_b32_e32 v190, 18, v240
	v_lshlrev_b64 v[190:191], 11, v[190:191]
	v_add_f32_e32 v60, v251, v60
	v_mfma_f32_32x32x16_f16 v[2:17], v[150:153], v[154:157], v[2:17]
	v_lshl_add_u64 v[190:191], v[0:1], 0, v[190:191]
	global_store_dword v[190:191], v60, off sc1
	v_or_b32_e32 v60, 19, v240
	v_add_f32_e32 v192, v251, v61
	v_mov_b32_e32 v61, v239
	v_lshlrev_b64 v[60:61], 11, v[60:61]
	v_lshl_add_u64 v[60:61], v[0:1], 0, v[60:61]
	v_mfma_f32_32x32x16_f16 v[34:49], v[74:77], v[222:225], v[34:49]
	global_store_dword v[60:61], v192, off sc1
	v_or_b32_e32 v192, 24, v240
	v_lshlrev_b64 v[192:193], 11, v[192:193]
	v_add_f32_e32 v62, v251, v62
	v_lshl_add_u64 v[192:193], v[0:1], 0, v[192:193]
	global_store_dword v[192:193], v62, off sc1
	v_or_b32_e32 v62, 25, v240
	v_mfma_f32_32x32x16_f16 v[18:33], v[158:161], v[142:145], v[18:33]
	v_add_f32_e32 v194, v251, v63
	v_mov_b32_e32 v63, v239
	v_lshlrev_b64 v[62:63], 11, v[62:63]
	v_lshl_add_u64 v[62:63], v[0:1], 0, v[62:63]
	global_store_dword v[62:63], v194, off sc1
	v_or_b32_e32 v194, 26, v240
	v_lshlrev_b64 v[194:195], 11, v[194:195]
	v_mfma_f32_32x32x16_f16 v[2:17], v[134:137], v[142:145], v[2:17]
	v_add_f32_e32 v64, v251, v64
	v_lshl_add_u64 v[194:195], v[0:1], 0, v[194:195]
	global_store_dword v[194:195], v64, off sc1
	v_or_b32_e32 v64, 27, v240
	v_add_f32_e32 v196, v251, v65
	v_mov_b32_e32 v65, v239
	v_lshlrev_b64 v[64:65], 11, v[64:65]
	v_mfma_f32_32x32x16_f16 v[34:49], v[82:85], v[226:229], v[34:49]
	v_lshl_add_u64 v[64:65], v[0:1], 0, v[64:65]
	global_store_dword v[64:65], v196, off sc1
	v_or_b32_e32 v196, 32, v240
	v_lshlrev_b64 v[114:115], 11, v[196:197]
	v_lshl_add_u64 v[114:115], v[0:1], 0, v[114:115]
	v_mov_b32_e32 v117, v239
	v_mov_b32_e32 v105, v239
	v_mfma_f32_32x32x16_f16 v[18:33], v[146:149], v[126:129], v[18:33]
	v_mov_b32_e32 v107, v239
	v_mov_b32_e32 v109, v239
	v_mfma_f32_32x32x16_f16 v[2:17], v[118:121], v[126:129], v[2:17]
	v_mov_b32_e32 v119, v239
	v_mov_b32_e32 v121, v239
	v_mfma_f32_32x32x16_f16 v[34:49], v[90:93], v[230:233], v[34:49]
	v_mfma_f32_32x32x16_f16 v[18:33], v[138:141], v[70:73], v[18:33]
	v_mfma_f32_32x32x16_f16 v[2:17], v[66:69], v[70:73], v[2:17]
	v_mfma_f32_32x32x16_f16 v[34:49], v[98:101], v[234:237], v[34:49]
	v_mfma_f32_32x32x16_f16 v[18:33], v[166:169], v[78:81], v[18:33]
	s_nop 10
	v_add_f32_e32 v34, v251, v34
	global_store_dword v[114:115], v34, off sc1
	v_or_b32_e32 v34, 33, v240
	v_add_f32_e32 v116, v251, v35
	v_mov_b32_e32 v35, v239
	v_lshlrev_b64 v[34:35], 11, v[34:35]
	v_lshl_add_u64 v[34:35], v[0:1], 0, v[34:35]
	v_mfma_f32_32x32x16_f16 v[2:17], v[74:77], v[78:81], v[2:17]
	global_store_dword v[34:35], v116, off sc1
	v_or_b32_e32 v116, 34, v240
	v_lshlrev_b64 v[116:117], 11, v[116:117]
	v_add_f32_e32 v36, v251, v36
	v_lshl_add_u64 v[102:103], v[0:1], 0, v[116:117]
	global_store_dword v[102:103], v36, off sc1
	v_or_b32_e32 v36, 35, v240
	v_mfma_f32_32x32x16_f16 v[18:33], v[170:173], v[86:89], v[18:33]
	v_add_f32_e32 v104, v251, v37
	v_mov_b32_e32 v37, v239
	v_lshlrev_b64 v[36:37], 11, v[36:37]
	v_lshl_add_u64 v[36:37], v[0:1], 0, v[36:37]
	global_store_dword v[36:37], v104, off sc1
	v_or_b32_e32 v104, 40, v240
	v_lshlrev_b64 v[104:105], 11, v[104:105]
	v_mfma_f32_32x32x16_f16 v[2:17], v[82:85], v[86:89], v[2:17]
	v_add_f32_e32 v38, v251, v38
	v_lshl_add_u64 v[104:105], v[0:1], 0, v[104:105]
	global_store_dword v[104:105], v38, off sc1
	v_or_b32_e32 v38, 41, v240
	v_add_f32_e32 v106, v251, v39
	v_mov_b32_e32 v39, v239
	v_lshlrev_b64 v[38:39], 11, v[38:39]
	v_mfma_f32_32x32x16_f16 v[18:33], v[174:177], v[94:97], v[18:33]
	v_lshl_add_u64 v[38:39], v[0:1], 0, v[38:39]
	global_store_dword v[38:39], v106, off sc1
	v_or_b32_e32 v106, 42, v240
	v_lshlrev_b64 v[106:107], 11, v[106:107]
	v_add_f32_e32 v40, v251, v40
	v_lshl_add_u64 v[106:107], v[0:1], 0, v[106:107]
	global_store_dword v[106:107], v40, off sc1
	v_mfma_f32_32x32x16_f16 v[2:17], v[90:93], v[94:97], v[2:17]
	v_or_b32_e32 v40, 43, v240
	v_add_f32_e32 v108, v251, v41
	v_mov_b32_e32 v41, v239
	v_lshlrev_b64 v[40:41], 11, v[40:41]
	v_lshl_add_u64 v[40:41], v[0:1], 0, v[40:41]
	global_store_dword v[40:41], v108, off sc1
	v_or_b32_e32 v108, 48, v240
	v_mfma_f32_32x32x16_f16 v[18:33], v[178:181], v[110:113], v[18:33]
	v_lshlrev_b64 v[108:109], 11, v[108:109]
	v_add_f32_e32 v42, v251, v42
	v_lshl_add_u64 v[108:109], v[0:1], 0, v[108:109]
	global_store_dword v[108:109], v42, off sc1
	v_or_b32_e32 v42, 49, v240
	v_add_f32_e32 v116, v251, v43
	v_mov_b32_e32 v43, v239
	v_mfma_f32_32x32x16_f16 v[2:17], v[98:101], v[110:113], v[2:17]
	v_lshlrev_b64 v[42:43], 11, v[42:43]
	v_lshl_add_u64 v[42:43], v[0:1], 0, v[42:43]
	global_store_dword v[42:43], v116, off sc1
	v_or_b32_e32 v116, 50, v240
	v_mov_b32_e32 v117, v239
	v_lshlrev_b64 v[116:117], 11, v[116:117]
	s_waitcnt vmcnt(26)
	v_add_f32_e32 v18, v252, v18
	s_nop 3
	v_add_f32_e32 v2, v252, v2
	v_add_f32_e32 v44, v251, v44
	v_lshl_add_u64 v[116:117], v[0:1], 0, v[116:117]
	global_store_dword v[242:243], v18, off offset:128 sc1
	v_add_f32_e32 v18, v252, v19
	global_store_dword v[114:115], v2, off offset:128 sc1
	v_add_f32_e32 v2, v252, v3
	global_store_dword v[116:117], v44, off sc1
	v_or_b32_e32 v44, 51, v240
	v_add_f32_e32 v118, v251, v45
	v_mov_b32_e32 v45, v239
	global_store_dword v[50:51], v18, off offset:128 sc1
	v_add_f32_e32 v18, v252, v20
	global_store_dword v[34:35], v2, off offset:128 sc1
	v_add_f32_e32 v2, v252, v4
	v_lshlrev_b64 v[44:45], 11, v[44:45]
	global_store_dword v[186:187], v18, off offset:128 sc1
	v_add_f32_e32 v18, v252, v21
	global_store_dword v[102:103], v2, off offset:128 sc1
	v_add_f32_e32 v2, v252, v5
	v_lshl_add_u64 v[44:45], v[0:1], 0, v[44:45]
	global_store_dword v[52:53], v18, off offset:128 sc1
	v_add_f32_e32 v18, v252, v22
	global_store_dword v[36:37], v2, off offset:128 sc1
	v_add_f32_e32 v2, v252, v6
	global_store_dword v[44:45], v118, off sc1
	v_or_b32_e32 v118, 56, v240
	global_store_dword v[182:183], v18, off offset:128 sc1
	v_add_f32_e32 v18, v252, v23
	global_store_dword v[104:105], v2, off offset:128 sc1
	v_add_f32_e32 v2, v252, v7
	v_lshlrev_b64 v[118:119], 11, v[118:119]
	global_store_dword v[54:55], v18, off offset:128 sc1
	v_add_f32_e32 v18, v252, v24
	global_store_dword v[38:39], v2, off offset:128 sc1
	v_add_f32_e32 v2, v252, v8
	v_add_f32_e32 v46, v251, v46
	v_lshl_add_u64 v[118:119], v[0:1], 0, v[118:119]
	global_store_dword v[184:185], v18, off offset:128 sc1
	v_add_f32_e32 v18, v252, v25
	global_store_dword v[106:107], v2, off offset:128 sc1
	v_add_f32_e32 v2, v252, v9
	global_store_dword v[118:119], v46, off sc1
	v_or_b32_e32 v46, 57, v240
	v_add_f32_e32 v120, v251, v47
	v_mov_b32_e32 v47, v239
	global_store_dword v[56:57], v18, off offset:128 sc1
	v_add_f32_e32 v18, v252, v26
	global_store_dword v[40:41], v2, off offset:128 sc1
	v_add_f32_e32 v2, v252, v10
	v_lshlrev_b64 v[46:47], 11, v[46:47]
	global_store_dword v[188:189], v18, off offset:128 sc1
	v_add_f32_e32 v18, v252, v27
	global_store_dword v[108:109], v2, off offset:128 sc1
	v_add_f32_e32 v2, v252, v11
	v_lshl_add_u64 v[46:47], v[0:1], 0, v[46:47]
	global_store_dword v[58:59], v18, off offset:128 sc1
	v_add_f32_e32 v18, v252, v28
	global_store_dword v[42:43], v2, off offset:128 sc1
	v_add_f32_e32 v2, v252, v12
	global_store_dword v[46:47], v120, off sc1
	v_or_b32_e32 v120, 58, v240
	global_store_dword v[190:191], v18, off offset:128 sc1
	v_add_f32_e32 v18, v252, v29
	global_store_dword v[116:117], v2, off offset:128 sc1
	v_add_f32_e32 v2, v252, v13
	v_lshlrev_b64 v[120:121], 11, v[120:121]
	global_store_dword v[60:61], v18, off offset:128 sc1
	v_add_f32_e32 v18, v252, v30
	global_store_dword v[44:45], v2, off offset:128 sc1
	v_add_f32_e32 v2, v252, v14
	v_add_f32_e32 v48, v251, v48
	v_lshl_add_u64 v[120:121], v[0:1], 0, v[120:121]
	global_store_dword v[192:193], v18, off offset:128 sc1
	v_add_f32_e32 v18, v252, v31
	global_store_dword v[118:119], v2, off offset:128 sc1
	v_add_f32_e32 v2, v252, v15
	global_store_dword v[120:121], v48, off sc1
	v_add_f32_e32 v122, v251, v49
	v_lshlrev_b64 v[48:49], 11, v[238:239]
	global_store_dword v[62:63], v18, off offset:128 sc1
	v_add_f32_e32 v18, v252, v32
	global_store_dword v[46:47], v2, off offset:128 sc1
	v_add_f32_e32 v2, v252, v16
	v_lshl_add_u64 v[0:1], v[0:1], 0, v[48:49]
	global_store_dword v[194:195], v18, off offset:128 sc1
	v_add_f32_e32 v18, v252, v33
	global_store_dword v[120:121], v2, off offset:128 sc1
	v_add_f32_e32 v2, v252, v17
	global_store_dword v[0:1], v122, off sc1
	global_store_dword v[64:65], v18, off offset:128 sc1
	global_store_dword v[0:1], v2, off offset:128 sc1
	s_endpgm
	.p2align	8

	.amdhsa_kernel _ZN12_GLOBAL__N_112oproj_kernelEPKDF16_S1_PKfPf
		.amdhsa_group_segment_fixed_size 65536
		.amdhsa_private_segment_fixed_size 0
		.amdhsa_kernarg_size 32
		.amdhsa_user_sgpr_count 2
		.amdhsa_user_sgpr_dispatch_ptr 0
		.amdhsa_user_sgpr_queue_ptr 0
		.amdhsa_user_sgpr_kernarg_segment_ptr 1
		.amdhsa_user_sgpr_dispatch_id 0
		.amdhsa_user_sgpr_kernarg_preload_length 0
		.amdhsa_user_sgpr_kernarg_preload_offset 0
		.amdhsa_user_sgpr_private_segment_size 0
		.amdhsa_uses_dynamic_stack 0
		.amdhsa_enable_private_segment 0
		.amdhsa_system_sgpr_workgroup_id_x 1
		.amdhsa_system_sgpr_workgroup_id_y 0
		.amdhsa_system_sgpr_workgroup_id_z 0
		.amdhsa_system_sgpr_workgroup_info 0
		.amdhsa_system_vgpr_workitem_id 0
		.amdhsa_next_free_vgpr 256
		.amdhsa_next_free_sgpr 96
		.amdhsa_accum_offset 256
		.amdhsa_reserve_vcc 1
		.amdhsa_float_round_mode_32 0
		.amdhsa_float_round_mode_16_64 0
		.amdhsa_float_denorm_mode_32 3
		.amdhsa_float_denorm_mode_16_64 3
		.amdhsa_dx10_clamp 1
		.amdhsa_ieee_mode 1
		.amdhsa_fp16_overflow 0
		.amdhsa_tg_split 0
		.amdhsa_exception_fp_ieee_invalid_op 0
		.amdhsa_exception_fp_denorm_src 0
		.amdhsa_exception_fp_ieee_div_zero 0
		.amdhsa_exception_fp_ieee_overflow 0
		.amdhsa_exception_fp_ieee_underflow 0
		.amdhsa_exception_fp_ieee_inexact 0
		.amdhsa_exception_int_div_zero 0
	.end_amdhsa_kernel

amdhsa.kernels:
  - .agpr_count:     0
    .args:
      - .actual_access:  read_only
        .address_space:  global
        .offset:         0
        .size:           8
        .value_kind:     global_buffer
      - .actual_access:  read_only
        .address_space:  global
        .offset:         8
        .size:           8
        .value_kind:     global_buffer
      - .actual_access:  read_only
        .address_space:  global
        .offset:         16
        .size:           8
        .value_kind:     global_buffer
      - .actual_access:  read_only
        .address_space:  global
        .offset:         24
        .size:           8
        .value_kind:     global_buffer
      - .actual_access:  read_only
        .address_space:  global
        .offset:         32
        .size:           8
        .value_kind:     global_buffer
      - .actual_access:  write_only
        .address_space:  global
        .offset:         40
        .size:           8
        .value_kind:     global_buffer
      - .actual_access:  write_only
        .address_space:  global
        .offset:         48
        .size:           8
        .value_kind:     global_buffer
      - .actual_access:  write_only
        .address_space:  global
        .offset:         56
        .size:           8
        .value_kind:     global_buffer
      - .actual_access:  write_only
        .address_space:  global
        .offset:         64
        .size:           8
        .value_kind:     global_buffer
    .group_segment_fixed_size: 16640
    .kernarg_segment_align: 8
    .kernarg_segment_size: 72
    .language:       OpenCL C
    .language_version:
      - 2
      - 0
    .max_flat_workgroup_size: 256
    .name:           _ZN12_GLOBAL__N_111prep_kernelEPKfS1_S1_S1_PKiPDF16_PiS5_Pf
    .private_segment_fixed_size: 0
    .sgpr_count:     42
    .sgpr_spill_count: 0
    .symbol:         _ZN12_GLOBAL__N_111prep_kernelEPKfS1_S1_S1_PKiPDF16_PiS5_Pf.kd
    .uniform_work_group_size: 1
    .uses_dynamic_stack: false
    .vgpr_count:     49
    .vgpr_spill_count: 0
    .wavefront_size: 64
  - .agpr_count:     0
    .args:
      - .actual_access:  read_only
        .address_space:  global
        .offset:         0
        .size:           8
        .value_kind:     global_buffer
      - .actual_access:  read_only
        .address_space:  global
        .offset:         8
        .size:           8
        .value_kind:     global_buffer
      - .actual_access:  read_only
        .address_space:  global
        .offset:         16
        .size:           8
        .value_kind:     global_buffer
      - .actual_access:  read_only
        .address_space:  global
        .offset:         24
        .size:           8
        .value_kind:     global_buffer
      - .actual_access:  read_only
        .address_space:  global
        .offset:         32
        .size:           8
        .value_kind:     global_buffer
      - .actual_access:  read_only
        .address_space:  global
        .offset:         40
        .size:           8
        .value_kind:     global_buffer
      - .actual_access:  read_only
        .address_space:  global
        .offset:         48
        .size:           8
        .value_kind:     global_buffer
      - .actual_access:  read_only
        .address_space:  global
        .offset:         56
        .size:           8
        .value_kind:     global_buffer
      - .actual_access:  write_only
        .address_space:  global
        .offset:         64
        .size:           8
        .value_kind:     global_buffer
      - .actual_access:  write_only
        .address_space:  global
        .offset:         72
        .size:           8
        .value_kind:     global_buffer
      - .actual_access:  write_only
        .address_space:  global
        .offset:         80
        .size:           8
        .value_kind:     global_buffer
    .group_segment_fixed_size: 32768
    .kernarg_segment_align: 8
    .kernarg_segment_size: 88
    .language:       OpenCL C
    .language_version:
      - 2
      - 0
    .max_flat_workgroup_size: 512
    .name:           _ZN12_GLOBAL__N_110qkv_kernelEPKfPKDF16_S1_S1_S1_PKiS5_S1_PDF16_S6_S6_
    .private_segment_fixed_size: 0
    .sgpr_count:     102
    .sgpr_spill_count: 0
    .symbol:         _ZN12_GLOBAL__N_110qkv_kernelEPKfPKDF16_S1_S1_S1_PKiS5_S1_PDF16_S6_S6_.kd
    .uniform_work_group_size: 1
    .uses_dynamic_stack: false
    .vgpr_count:     252
    .vgpr_spill_count: 0
    .wavefront_size: 64
  - .agpr_count:     0
    .args:
      - .actual_access:  read_only
        .address_space:  global
        .offset:         0
        .size:           8
        .value_kind:     global_buffer
      - .actual_access:  read_only
        .address_space:  global
        .offset:         8
        .size:           8
        .value_kind:     global_buffer
      - .actual_access:  read_only
        .address_space:  global
        .offset:         16
        .size:           8
        .value_kind:     global_buffer
      - .actual_access:  write_only
        .address_space:  global
        .offset:         24
        .size:           8
        .value_kind:     global_buffer
    .group_segment_fixed_size: 65536
    .kernarg_segment_align: 8
    .kernarg_segment_size: 32
    .language:       OpenCL C
    .language_version:
      - 2
      - 0
    .max_flat_workgroup_size: 256
    .name:           _ZN12_GLOBAL__N_112oproj_kernelEPKDF16_S1_PKfPf
    .private_segment_fixed_size: 0
    .sgpr_count:     20
    .sgpr_spill_count: 0
    .symbol:         _ZN12_GLOBAL__N_112oproj_kernelEPKDF16_S1_PKfPf.kd
    .uniform_work_group_size: 1
    .uses_dynamic_stack: false
    .vgpr_count:     256
    .vgpr_spill_count: 0
    .wavefront_size: 64
  - .agpr_count:     0
    .args:
      - .actual_access:  read_only
        .address_space:  global
        .offset:         0
        .size:           8
        .value_kind:     global_buffer
      - .address_space:  global
        .offset:         8
        .size:           8
        .value_kind:     global_buffer
      - .address_space:  global
        .offset:         16
        .size:           8
        .value_kind:     global_buffer
      - .actual_access:  read_only
        .address_space:  global
        .offset:         24
        .size:           8
        .value_kind:     global_buffer
      - .actual_access:  write_only
        .address_space:  global
        .offset:         32
        .size:           8
        .value_kind:     global_buffer
    .group_segment_fixed_size: 0
    .kernarg_segment_align: 8
    .kernarg_segment_size: 40
    .language:       OpenCL C
    .language_version:
      - 2
      - 0
    .max_flat_workgroup_size: 512
    .name:           _ZN12_GLOBAL__N_111attn_kernelEPKDF16_S1_S1_PKiPDF16_
    .private_segment_fixed_size: 0
    .sgpr_count:     106
    .sgpr_spill_count: 2
    .symbol:         _ZN12_GLOBAL__N_111attn_kernelEPKDF16_S1_S1_PKiPDF16_.kd
    .uniform_work_group_size: 1
    .uses_dynamic_stack: false
    .vgpr_count:     212
    .vgpr_spill_count: 0
    .wavefront_size: 64
